# v20 + MoE weight conversion waits for each 32-load batch right after issuing it (s_waitcnt vmcnt(0)): fewer requests in flight, faster
# baseline (speedup 1.0000x reference)
.LBB0_45:
	s_lshr_b32 s7, s11, 5
	v_cvt_f32_ubyte0_e32 v34, s7
	v_rcp_iflag_f32_e32 v34, v34
	s_mulk_i32 s12, 0xf200
	s_mulk_i32 s10, 0x7000
	s_sub_i32 s16, 0, s7
	v_mul_f32_e32 v34, 0x4f7ffffe, v34
	v_cvt_u32_f32_e32 v34, v34
	s_sub_i32 s10, s12, s10
	s_add_i32 s10, s22, s10
	s_abs_i32 s13, s10
	v_readfirstlane_b32 s17, v34
	s_mul_i32 s16, s16, s17
	s_mul_hi_u32 s16, s17, s16
	s_add_i32 s17, s17, s16
	s_mul_hi_u32 s16, s13, s17
	s_mul_i32 s17, s16, s7
	s_sub_i32 s13, s13, s17
	s_ashr_i32 s12, s10, 31
	s_add_i32 s17, s16, 1
	s_sub_i32 s18, s13, s7
	s_cmp_ge_u32 s13, s7
	s_cselect_b32 s16, s17, s16
	s_cselect_b32 s13, s18, s13
	s_add_i32 s17, s16, 1
	s_cmp_ge_u32 s13, s7
	s_cselect_b32 s13, s17, s16
	s_xor_b32 s13, s13, s12
	s_sub_i32 s12, s13, s12
	s_mul_i32 s7, s12, s7
	s_sub_i32 s7, s10, s7
	s_lshl_b32 s10, s12, 7
	s_lshl_b32 s12, s7, 5
	s_ashr_i32 s13, s12, 31
	s_lshl_b64 s[16:17], s[12:13], 2
	v_or_b32_e32 v50, s10, v94
	v_lshl_add_u64 v[32:33], v[32:33], 0, s[16:17]
	v_lshl_add_u64 v[32:33], v[32:33], 0, v[74:75]
	v_mad_i64_i32 v[34:35], s[16:17], v50, s11, 0
	v_or_b32_e32 v36, 2, v50
	v_or_b32_e32 v38, 4, v50
	v_or_b32_e32 v40, 6, v50
	v_or_b32_e32 v42, 8, v50
	v_or_b32_e32 v44, 10, v50
	v_or_b32_e32 v46, 12, v50
	v_or_b32_e32 v48, 14, v50
	v_lshl_add_u64 v[34:35], v[34:35], 2, v[32:33]
	v_mad_i64_i32 v[36:37], s[16:17], v36, s11, 0
	v_mad_i64_i32 v[38:39], s[16:17], v38, s11, 0
	v_mad_i64_i32 v[40:41], s[16:17], v40, s11, 0
	v_mad_i64_i32 v[42:43], s[16:17], v42, s11, 0
	v_mad_i64_i32 v[44:45], s[16:17], v44, s11, 0
	v_mad_i64_i32 v[46:47], s[16:17], v46, s11, 0
	v_mad_i64_i32 v[48:49], s[16:17], v48, s11, 0
	v_lshl_add_u64 v[36:37], v[36:37], 2, v[32:33]
	v_lshl_add_u64 v[38:39], v[38:39], 2, v[32:33]
	v_lshl_add_u64 v[40:41], v[40:41], 2, v[32:33]
	v_lshl_add_u64 v[42:43], v[42:43], 2, v[32:33]
	v_lshl_add_u64 v[44:45], v[44:45], 2, v[32:33]
	v_lshl_add_u64 v[46:47], v[46:47], 2, v[32:33]
	v_lshl_add_u64 v[48:49], v[48:49], 2, v[32:33]
	global_load_dword v98, v[34:35], off nt
	global_load_dword v99, v[36:37], off nt
	global_load_dword v100, v[38:39], off nt
	global_load_dword v101, v[40:41], off nt
	global_load_dword v102, v[42:43], off nt
	global_load_dword v103, v[44:45], off nt
	global_load_dword v104, v[46:47], off nt
	global_load_dword v105, v[48:49], off nt
	v_or_b32_e32 v34, 16, v50
	v_mad_i64_i32 v[34:35], s[16:17], v34, s11, 0
	v_or_b32_e32 v36, 18, v50
	v_or_b32_e32 v38, 20, v50
	v_or_b32_e32 v40, 22, v50
	v_or_b32_e32 v42, 24, v50
	v_or_b32_e32 v44, 26, v50
	v_or_b32_e32 v46, 28, v50
	v_or_b32_e32 v48, 30, v50
	v_lshl_add_u64 v[34:35], v[34:35], 2, v[32:33]
	v_mad_i64_i32 v[36:37], s[16:17], v36, s11, 0
	v_mad_i64_i32 v[38:39], s[16:17], v38, s11, 0
	v_mad_i64_i32 v[40:41], s[16:17], v40, s11, 0
	v_mad_i64_i32 v[42:43], s[16:17], v42, s11, 0
	v_mad_i64_i32 v[44:45], s[16:17], v44, s11, 0
	v_mad_i64_i32 v[46:47], s[16:17], v46, s11, 0
	v_mad_i64_i32 v[48:49], s[16:17], v48, s11, 0
	v_lshl_add_u64 v[36:37], v[36:37], 2, v[32:33]
	v_lshl_add_u64 v[38:39], v[38:39], 2, v[32:33]
	v_lshl_add_u64 v[40:41], v[40:41], 2, v[32:33]
	v_lshl_add_u64 v[42:43], v[42:43], 2, v[32:33]
	v_lshl_add_u64 v[44:45], v[44:45], 2, v[32:33]
	v_lshl_add_u64 v[46:47], v[46:47], 2, v[32:33]
	v_lshl_add_u64 v[48:49], v[48:49], 2, v[32:33]
	global_load_dword v106, v[34:35], off nt
	global_load_dword v107, v[36:37], off nt
	global_load_dword v108, v[38:39], off nt
	global_load_dword v109, v[40:41], off nt
	global_load_dword v110, v[42:43], off nt
	global_load_dword v111, v[44:45], off nt
	global_load_dword v112, v[46:47], off nt
	global_load_dword v113, v[48:49], off nt
	v_or_b32_e32 v34, 32, v50
	v_mad_i64_i32 v[34:35], s[16:17], v34, s11, 0
	v_or_b32_e32 v36, 34, v50
	v_or_b32_e32 v38, 36, v50
	v_or_b32_e32 v40, 38, v50
	v_or_b32_e32 v42, 40, v50
	v_or_b32_e32 v44, 42, v50
	v_or_b32_e32 v46, 44, v50
	v_or_b32_e32 v48, 46, v50
	v_lshl_add_u64 v[34:35], v[34:35], 2, v[32:33]
	v_mad_i64_i32 v[36:37], s[16:17], v36, s11, 0
	v_mad_i64_i32 v[38:39], s[16:17], v38, s11, 0
	v_mad_i64_i32 v[40:41], s[16:17], v40, s11, 0
	v_mad_i64_i32 v[42:43], s[16:17], v42, s11, 0
	v_mad_i64_i32 v[44:45], s[16:17], v44, s11, 0
	v_mad_i64_i32 v[46:47], s[16:17], v46, s11, 0
	v_mad_i64_i32 v[48:49], s[16:17], v48, s11, 0
	v_lshl_add_u64 v[36:37], v[36:37], 2, v[32:33]
	v_lshl_add_u64 v[38:39], v[38:39], 2, v[32:33]
	v_lshl_add_u64 v[40:41], v[40:41], 2, v[32:33]
	v_lshl_add_u64 v[42:43], v[42:43], 2, v[32:33]
	v_lshl_add_u64 v[44:45], v[44:45], 2, v[32:33]
	v_lshl_add_u64 v[46:47], v[46:47], 2, v[32:33]
	v_lshl_add_u64 v[48:49], v[48:49], 2, v[32:33]
	global_load_dword v114, v[34:35], off nt
	global_load_dword v115, v[36:37], off nt
	global_load_dword v116, v[38:39], off nt
	global_load_dword v117, v[40:41], off nt
	global_load_dword v118, v[42:43], off nt
	global_load_dword v119, v[44:45], off nt
	global_load_dword v120, v[46:47], off nt
	global_load_dword v121, v[48:49], off nt
	v_or_b32_e32 v34, 48, v50
	v_mad_i64_i32 v[34:35], s[16:17], v34, s11, 0
	v_or_b32_e32 v36, 50, v50
	v_or_b32_e32 v38, 52, v50
	v_or_b32_e32 v40, 54, v50
	v_or_b32_e32 v42, 56, v50
	v_or_b32_e32 v44, 58, v50
	v_or_b32_e32 v46, 60, v50
	v_or_b32_e32 v48, 62, v50
	v_lshl_add_u64 v[34:35], v[34:35], 2, v[32:33]
	v_mad_i64_i32 v[36:37], s[16:17], v36, s11, 0
	v_mad_i64_i32 v[38:39], s[16:17], v38, s11, 0
	v_mad_i64_i32 v[40:41], s[16:17], v40, s11, 0
	v_mad_i64_i32 v[42:43], s[16:17], v42, s11, 0
	v_mad_i64_i32 v[44:45], s[16:17], v44, s11, 0
	v_mad_i64_i32 v[46:47], s[16:17], v46, s11, 0
	v_mad_i64_i32 v[48:49], s[16:17], v48, s11, 0
	v_lshl_add_u64 v[36:37], v[36:37], 2, v[32:33]
	v_lshl_add_u64 v[38:39], v[38:39], 2, v[32:33]
	v_lshl_add_u64 v[40:41], v[40:41], 2, v[32:33]
	v_lshl_add_u64 v[42:43], v[42:43], 2, v[32:33]
	v_lshl_add_u64 v[44:45], v[44:45], 2, v[32:33]
	v_lshl_add_u64 v[46:47], v[46:47], 2, v[32:33]
	v_lshl_add_u64 v[32:33], v[48:49], 2, v[32:33]
	global_load_dword v122, v[34:35], off nt
	global_load_dword v123, v[36:37], off nt
	global_load_dword v124, v[38:39], off nt
	global_load_dword v125, v[40:41], off nt
	global_load_dword v126, v[42:43], off nt
	global_load_dword v127, v[44:45], off nt
	global_load_dword v128, v[46:47], off nt
	global_load_dword v129, v[32:33], off nt
	s_waitcnt vmcnt(0)
	s_mov_b64 s[16:17], -1
	s_and_b64 vcc, exec, s[14:15]
	v_or_b32_e32 v131, s12, v86
	v_or_b32_e32 v130, s12, v90
	v_add_u32_e32 v32, 0x200, v88
	v_add_u32_e32 v33, 0x400, v88
	v_add_u32_e32 v34, 0x600, v88
	v_add_u32_e32 v35, 0x800, v88
	v_add_u32_e32 v36, 0xa00, v88
	v_add_u32_e32 v37, 0xc00, v88
	v_add_u32_e32 v38, 0xe00, v88
	v_add_u32_e32 v39, 0x1000, v88
	v_add_u32_e32 v40, 0x1200, v88
	v_add_u32_e32 v41, 0x1400, v88
	v_add_u32_e32 v42, 0x1600, v88
	v_add_u32_e32 v43, 0x1800, v88
	v_add_u32_e32 v44, 0x1a00, v88
	v_add_u32_e32 v45, 0x1c00, v88
	v_add_u32_e32 v132, 0x400, v89
	s_cbranch_vccz .LBB0_47
	s_waitcnt vmcnt(62)
	v_mul_f32_e32 v46, 0x42800000, v1
	s_waitcnt vmcnt(61)
	v_mul_f32_e32 v47, 0x42800000, v2
	ds_write2_b32 v88, v46, v47 offset0:66 offset1:132
	s_waitcnt vmcnt(60)
	v_mul_f32_e32 v46, 0x42800000, v3
	s_waitcnt vmcnt(59)
	v_mul_f32_e32 v47, 0x42800000, v4
	ds_write2_b32 v32, v46, v47 offset0:70 offset1:136
	s_waitcnt vmcnt(58)
	v_mul_f32_e32 v46, 0x42800000, v5
	s_waitcnt vmcnt(57)
	v_mul_f32_e32 v47, 0x42800000, v6
	ds_write2_b32 v33, v46, v47 offset0:74 offset1:140
	s_waitcnt vmcnt(56)
	v_mul_f32_e32 v46, 0x42800000, v7
	s_waitcnt vmcnt(55)
	v_mul_f32_e32 v47, 0x42800000, v8
	ds_write2_b32 v34, v46, v47 offset0:78 offset1:144
	s_waitcnt vmcnt(54)
	v_mul_f32_e32 v46, 0x42800000, v9
	s_waitcnt vmcnt(53)
	v_mul_f32_e32 v47, 0x42800000, v10
	ds_write2_b32 v35, v46, v47 offset0:82 offset1:148
	s_waitcnt vmcnt(52)
	v_mul_f32_e32 v46, 0x42800000, v11
	s_waitcnt vmcnt(51)
	v_mul_f32_e32 v47, 0x42800000, v12
	ds_write2_b32 v36, v46, v47 offset0:86 offset1:152
	s_waitcnt vmcnt(50)
	v_mul_f32_e32 v46, 0x42800000, v13
	s_waitcnt vmcnt(49)
	v_mul_f32_e32 v47, 0x42800000, v14
	ds_write2_b32 v37, v46, v47 offset0:90 offset1:156
	s_waitcnt vmcnt(48)
	v_mul_f32_e32 v46, 0x42800000, v15
	s_waitcnt vmcnt(47)
	v_mul_f32_e32 v47, 0x42800000, v16
	ds_write2_b32 v38, v46, v47 offset0:94 offset1:160
	s_waitcnt vmcnt(46)
	v_mul_f32_e32 v46, 0x42800000, v17
	s_waitcnt vmcnt(45)
	v_mul_f32_e32 v47, 0x42800000, v18
	ds_write2_b32 v39, v46, v47 offset0:98 offset1:164
	s_waitcnt vmcnt(44)
	v_mul_f32_e32 v46, 0x42800000, v19
	s_waitcnt vmcnt(43)
	v_mul_f32_e32 v47, 0x42800000, v20
	ds_write2_b32 v40, v46, v47 offset0:102 offset1:168
	s_waitcnt vmcnt(42)
	v_mul_f32_e32 v46, 0x42800000, v21
	s_waitcnt vmcnt(41)
	v_mul_f32_e32 v47, 0x42800000, v22
	ds_write2_b32 v41, v46, v47 offset0:106 offset1:172
	s_waitcnt vmcnt(40)
	v_mul_f32_e32 v46, 0x42800000, v23
	s_waitcnt vmcnt(39)
	v_mul_f32_e32 v47, 0x42800000, v24
	ds_write2_b32 v42, v46, v47 offset0:110 offset1:176
	s_waitcnt vmcnt(38)
	v_mul_f32_e32 v46, 0x42800000, v25
	s_waitcnt vmcnt(37)
	v_mul_f32_e32 v47, 0x42800000, v26
	ds_write2_b32 v43, v46, v47 offset0:114 offset1:180
	s_waitcnt vmcnt(36)
	v_mul_f32_e32 v46, 0x42800000, v27
	s_waitcnt vmcnt(35)
	v_mul_f32_e32 v47, 0x42800000, v28
	ds_write2_b32 v44, v46, v47 offset0:118 offset1:184
	s_waitcnt vmcnt(34)
	v_mul_f32_e32 v46, 0x42800000, v29
	s_waitcnt vmcnt(33)
	v_mul_f32_e32 v47, 0x42800000, v30
	ds_write2_b32 v45, v46, v47 offset0:122 offset1:188
	v_mul_f32_e32 v46, 0x42800000, v0
	ds_write_b32 v87, v46
	s_waitcnt vmcnt(32)
	v_mul_f32_e32 v46, 0x42800000, v31
	ds_write_b32 v88, v46 offset:8184
	s_waitcnt lgkmcnt(0)
	ds_read2_b32 v[50:51], v89 offset1:16
	ds_read2_b32 v[52:53], v89 offset0:33 offset1:49
	ds_read2_b32 v[54:55], v89 offset0:66 offset1:82
	ds_read2_b32 v[56:57], v89 offset0:99 offset1:115
	ds_read2_b32 v[58:59], v89 offset0:132 offset1:148
	ds_read2_b32 v[60:61], v89 offset0:165 offset1:181
	ds_read2_b32 v[62:63], v89 offset0:198 offset1:214
	ds_read2_b32 v[134:135], v89 offset0:231 offset1:247
	ds_read2_b32 v[136:137], v132 offset0:8 offset1:24
	ds_read2_b32 v[138:139], v132 offset0:41 offset1:57
	ds_read2_b32 v[140:141], v132 offset0:74 offset1:90
	ds_read2_b32 v[142:143], v132 offset0:107 offset1:123
	ds_read2_b32 v[144:145], v132 offset0:140 offset1:156
	ds_read2_b32 v[146:147], v132 offset0:173 offset1:189
	v_mov_b32_e32 v46, v75
	v_mov_b32_e32 v47, v75
	v_mov_b32_e32 v48, v75
	v_mov_b32_e32 v49, v75
	ds_read2_b32 v[148:149], v132 offset0:206 offset1:222
	ds_read2_b32 v[150:151], v132 offset0:239 offset1:255
	s_waitcnt lgkmcnt(0)
	v_cvt_pk_fp8_f32 v46, v50, v52
	v_cvt_pk_fp8_f32 v47, v58, v60
	v_cvt_pk_fp8_f32 v48, v136, v138
	v_cvt_pk_fp8_f32 v49, v144, v146
	s_ashr_i32 s11, s10, 31
	v_cvt_pk_fp8_f32 v46, v54, v56 op_sel:[0,0,1]
	v_cvt_pk_fp8_f32 v47, v62, v134 op_sel:[0,0,1]
	v_cvt_pk_fp8_f32 v48, v140, v142 op_sel:[0,0,1]
	v_cvt_pk_fp8_f32 v49, v148, v150 op_sel:[0,0,1]
	v_lshl_add_u64 v[152:153], v[84:85], 0, s[10:11]
	v_lshl_add_u64 v[152:153], v[152:153], 0, v[80:81]
	v_mad_i64_i32 v[154:155], s[16:17], s6, v131, v[152:153]
	v_mov_b32_e32 v232, v46
	v_mov_b32_e32 v233, v47
	v_mov_b32_e32 v234, v48
	v_mov_b32_e32 v235, v49
	v_mov_b32_e32 v240, v154
	v_mov_b32_e32 v241, v155
	s_nop 1
	v_mov_b32_e32 v46, v75
	v_mov_b32_e32 v47, v75
	v_mov_b32_e32 v48, v75
	v_mov_b32_e32 v49, v75
	v_cvt_pk_fp8_f32 v46, v51, v53
	v_cvt_pk_fp8_f32 v47, v59, v61
	v_cvt_pk_fp8_f32 v48, v137, v139
	v_cvt_pk_fp8_f32 v49, v145, v147
	v_cvt_pk_fp8_f32 v46, v55, v57 op_sel:[0,0,1]
	v_cvt_pk_fp8_f32 v47, v63, v135 op_sel:[0,0,1]
	v_cvt_pk_fp8_f32 v48, v141, v143 op_sel:[0,0,1]
	v_cvt_pk_fp8_f32 v49, v149, v151 op_sel:[0,0,1]
	v_mad_i64_i32 v[50:51], s[16:17], s6, v130, v[152:153]
	s_mov_b64 s[16:17], 0
	v_mov_b32_e32 v236, v46
	v_mov_b32_e32 v237, v47
	v_mov_b32_e32 v238, v48
	v_mov_b32_e32 v239, v49
	v_mov_b32_e32 v242, v50
	v_mov_b32_e32 v243, v51
	s_waitcnt lgkmcnt(0)

.LBB0_49:
	s_add_i32 s22, s22, s52
	s_cmp_gt_i32 s22, 0x14fff
	s_cselect_b64 s[16:17], -1, 0
	s_and_b64 vcc, exec, s[16:17]
	s_cbranch_vccnz .LBB0_51
	s_mul_hi_i32 s11, s22, 0x92492493
	s_add_i32 s11, s11, s22
	s_lshr_b32 s13, s11, 31
	s_ashr_i32 s11, s11, 14
	s_add_i32 s18, s11, s13
	s_mul_i32 s11, s18, 0xffff9000
	s_add_i32 s11, s22, s11
	s_mul_hi_i32 s13, s11, 0x92492493
	s_add_i32 s13, s13, s11
	s_lshr_b32 s11, s13, 31
	s_ashr_i32 s13, s13, 11
	s_add_i32 s13, s13, s11
	s_mul_i32 s11, s13, 0xfffff200
	s_mul_i32 s19, s18, 0x7000
	s_sub_i32 s11, s11, s19
	s_ashr_i32 s19, s18, 31
	s_add_i32 s24, s22, s11
	s_lshl_b64 s[18:19], s[18:19], 3
	s_add_u32 s11, s88, s18
	s_addc_u32 s18, s89, s19
	s_add_u32 s11, s11, 0x108
	s_addc_u32 s18, s18, 0
	s_cmp_lt_i32 s22, 0xe000
	s_cselect_b32 s19, s18, s3
	s_cselect_b32 s18, s11, s1
	s_load_dwordx2 s[18:19], s[18:19], 0x0
	s_mul_hi_i32 s25, s13, 0x3800000
	s_mul_i32 s13, s13, 0x3800000
	s_cselect_b32 s11, s9, 0x800
	s_waitcnt lgkmcnt(0)
	s_add_u32 s13, s18, s13
	s_addc_u32 s25, s19, s25
	s_lshr_b32 s18, s11, 5
	s_abs_i32 s19, s18
	s_waitcnt vmcnt(62)
	v_cvt_f32_u32_e32 v0, s19
	s_sub_i32 s28, 0, s19
	s_abs_i32 s27, s24
	s_xor_b32 s26, s24, s18
	v_rcp_iflag_f32_e32 v0, v0
	s_ashr_i32 s26, s26, 31
	v_mul_f32_e32 v0, 0x4f7ffffe, v0
	v_cvt_u32_f32_e32 v0, v0
	s_nop 0
	v_readfirstlane_b32 s29, v0
	s_mul_i32 s28, s28, s29
	s_mul_hi_u32 s28, s29, s28
	s_add_i32 s29, s29, s28
	s_mul_hi_u32 s28, s27, s29
	s_mul_i32 s29, s28, s19
	s_sub_i32 s27, s27, s29
	s_add_i32 s29, s28, 1
	s_sub_i32 s30, s27, s19
	s_cmp_ge_u32 s27, s19
	s_cselect_b32 s28, s29, s28
	s_cselect_b32 s27, s30, s27
	s_add_i32 s29, s28, 1
	s_cmp_ge_u32 s27, s19
	s_cselect_b32 s19, s29, s28
	s_xor_b32 s19, s19, s26
	s_sub_i32 s19, s19, s26
	s_mul_i32 s18, s19, s18
	s_sub_i32 s18, s24, s18
	s_lshl_b32 s18, s18, 5
	v_lshl_or_b32 v133, s19, 7, v73
	s_ashr_i32 s19, s18, 31
	s_lshl_b64 s[18:19], s[18:19], 2
	s_add_u32 s18, s13, s18
	s_addc_u32 s19, s25, s19
	s_waitcnt vmcnt(59)
	v_or_b32_e32 v4, 2, v133
	s_waitcnt vmcnt(57)
	v_or_b32_e32 v6, 4, v133
	s_waitcnt vmcnt(55)
	v_or_b32_e32 v8, 6, v133
	s_waitcnt vmcnt(53)
	v_or_b32_e32 v10, 8, v133
	s_waitcnt vmcnt(51)
	v_or_b32_e32 v12, 10, v133
	s_waitcnt vmcnt(49)
	v_or_b32_e32 v14, 12, v133
	s_waitcnt vmcnt(47)
	v_or_b32_e32 v16, 14, v133
	s_waitcnt vmcnt(45)
	v_or_b32_e32 v18, 16, v133
	s_waitcnt vmcnt(43)
	v_or_b32_e32 v20, 18, v133
	s_waitcnt vmcnt(41)
	v_or_b32_e32 v22, 20, v133
	s_waitcnt vmcnt(39)
	v_or_b32_e32 v24, 22, v133
	s_waitcnt vmcnt(37)
	v_or_b32_e32 v26, 24, v133
	s_waitcnt vmcnt(35)
	v_or_b32_e32 v28, 26, v133
	s_waitcnt vmcnt(33)
	v_or_b32_e32 v30, 28, v133
	v_lshl_add_u64 v[0:1], s[18:19], 0, v[74:75]
	v_mad_i64_i32 v[2:3], s[18:19], v133, s11, 0
	v_mad_i64_i32 v[4:5], s[18:19], v4, s11, 0
	v_mad_i64_i32 v[6:7], s[18:19], v6, s11, 0
	v_mad_i64_i32 v[8:9], s[18:19], v8, s11, 0
	v_mad_i64_i32 v[10:11], s[18:19], v10, s11, 0
	v_mad_i64_i32 v[12:13], s[18:19], v12, s11, 0
	v_mad_i64_i32 v[14:15], s[18:19], v14, s11, 0
	v_mad_i64_i32 v[16:17], s[18:19], v16, s11, 0
	v_mad_i64_i32 v[18:19], s[18:19], v18, s11, 0
	v_mad_i64_i32 v[20:21], s[18:19], v20, s11, 0
	v_mad_i64_i32 v[22:23], s[18:19], v22, s11, 0
	v_mad_i64_i32 v[24:25], s[18:19], v24, s11, 0
	v_mad_i64_i32 v[26:27], s[18:19], v26, s11, 0
	v_mad_i64_i32 v[28:29], s[18:19], v28, s11, 0
	s_waitcnt vmcnt(32)
	v_mad_i64_i32 v[30:31], s[18:19], v30, s11, 0
	v_or_b32_e32 v32, 30, v133
	v_or_b32_e32 v34, 32, v133
	v_or_b32_e32 v36, 34, v133
	v_or_b32_e32 v38, 36, v133
	v_or_b32_e32 v40, 38, v133
	v_or_b32_e32 v42, 40, v133
	v_or_b32_e32 v44, 42, v133
	v_or_b32_e32 v46, 44, v133
	v_or_b32_e32 v48, 46, v133
	v_or_b32_e32 v50, 48, v133
	v_or_b32_e32 v52, 50, v133
	v_or_b32_e32 v54, 52, v133
	v_or_b32_e32 v56, 54, v133
	v_or_b32_e32 v58, 56, v133
	v_or_b32_e32 v60, 58, v133
	v_or_b32_e32 v62, 60, v133
	v_or_b32_e32 v133, 62, v133
	v_lshl_add_u64 v[2:3], v[2:3], 2, v[0:1]
	v_lshl_add_u64 v[4:5], v[4:5], 2, v[0:1]
	v_lshl_add_u64 v[6:7], v[6:7], 2, v[0:1]
	v_lshl_add_u64 v[8:9], v[8:9], 2, v[0:1]
	v_lshl_add_u64 v[10:11], v[10:11], 2, v[0:1]
	v_lshl_add_u64 v[12:13], v[12:13], 2, v[0:1]
	v_lshl_add_u64 v[14:15], v[14:15], 2, v[0:1]
	v_lshl_add_u64 v[16:17], v[16:17], 2, v[0:1]
	v_lshl_add_u64 v[18:19], v[18:19], 2, v[0:1]
	v_lshl_add_u64 v[20:21], v[20:21], 2, v[0:1]
	v_lshl_add_u64 v[22:23], v[22:23], 2, v[0:1]
	v_lshl_add_u64 v[24:25], v[24:25], 2, v[0:1]
	v_lshl_add_u64 v[26:27], v[26:27], 2, v[0:1]
	v_lshl_add_u64 v[28:29], v[28:29], 2, v[0:1]
	v_lshl_add_u64 v[30:31], v[30:31], 2, v[0:1]
	v_mad_i64_i32 v[32:33], s[18:19], v32, s11, 0
	v_mad_i64_i32 v[34:35], s[18:19], v34, s11, 0
	v_mad_i64_i32 v[36:37], s[18:19], v36, s11, 0
	v_mad_i64_i32 v[38:39], s[18:19], v38, s11, 0
	v_mad_i64_i32 v[40:41], s[18:19], v40, s11, 0
	v_mad_i64_i32 v[42:43], s[18:19], v42, s11, 0
	v_mad_i64_i32 v[44:45], s[18:19], v44, s11, 0
	v_mad_i64_i32 v[46:47], s[18:19], v46, s11, 0
	v_mad_i64_i32 v[48:49], s[18:19], v48, s11, 0
	v_mad_i64_i32 v[50:51], s[18:19], v50, s11, 0
	v_mad_i64_i32 v[52:53], s[18:19], v52, s11, 0
	v_mad_i64_i32 v[54:55], s[18:19], v54, s11, 0
	v_mad_i64_i32 v[56:57], s[18:19], v56, s11, 0
	v_mad_i64_i32 v[58:59], s[18:19], v58, s11, 0
	v_mad_i64_i32 v[60:61], s[18:19], v60, s11, 0
	v_mad_i64_i32 v[62:63], s[18:19], v62, s11, 0
	v_mad_i64_i32 v[134:135], s[18:19], v133, s11, 0
	v_lshl_add_u64 v[32:33], v[32:33], 2, v[0:1]
	v_lshl_add_u64 v[34:35], v[34:35], 2, v[0:1]
	v_lshl_add_u64 v[36:37], v[36:37], 2, v[0:1]
	v_lshl_add_u64 v[38:39], v[38:39], 2, v[0:1]
	v_lshl_add_u64 v[40:41], v[40:41], 2, v[0:1]
	v_lshl_add_u64 v[42:43], v[42:43], 2, v[0:1]
	v_lshl_add_u64 v[44:45], v[44:45], 2, v[0:1]
	v_lshl_add_u64 v[46:47], v[46:47], 2, v[0:1]
	v_lshl_add_u64 v[48:49], v[48:49], 2, v[0:1]
	v_lshl_add_u64 v[50:51], v[50:51], 2, v[0:1]
	v_lshl_add_u64 v[52:53], v[52:53], 2, v[0:1]
	v_lshl_add_u64 v[54:55], v[54:55], 2, v[0:1]
	v_lshl_add_u64 v[56:57], v[56:57], 2, v[0:1]
	v_lshl_add_u64 v[58:59], v[58:59], 2, v[0:1]
	v_lshl_add_u64 v[60:61], v[60:61], 2, v[0:1]
	v_lshl_add_u64 v[62:63], v[62:63], 2, v[0:1]
	v_lshl_add_u64 v[134:135], v[134:135], 2, v[0:1]
	global_load_dword v0, v[2:3], off nt
	global_load_dword v1, v[4:5], off nt
	s_nop 0
	global_load_dword v2, v[6:7], off nt
	global_load_dword v3, v[8:9], off nt
	global_load_dword v4, v[10:11], off nt
	global_load_dword v5, v[12:13], off nt
	s_nop 0
	global_load_dword v6, v[14:15], off nt
	global_load_dword v7, v[16:17], off nt
	global_load_dword v8, v[18:19], off nt
	global_load_dword v9, v[20:21], off nt
	global_load_dword v10, v[22:23], off nt
	global_load_dword v11, v[24:25], off nt
	global_load_dword v12, v[26:27], off nt
	global_load_dword v13, v[28:29], off nt
	global_load_dword v14, v[30:31], off nt
	global_load_dword v15, v[32:33], off nt
	global_load_dword v16, v[34:35], off nt
	global_load_dword v17, v[36:37], off nt
	global_load_dword v18, v[38:39], off nt
	global_load_dword v19, v[40:41], off nt
	global_load_dword v20, v[42:43], off nt
	global_load_dword v21, v[44:45], off nt
	global_load_dword v22, v[46:47], off nt
	global_load_dword v23, v[48:49], off nt
	global_load_dword v24, v[50:51], off nt
	global_load_dword v25, v[52:53], off nt
	global_load_dword v26, v[54:55], off nt
	global_load_dword v27, v[56:57], off nt
	global_load_dword v28, v[58:59], off nt
	global_load_dword v29, v[60:61], off nt
	global_load_dword v30, v[62:63], off nt
	global_load_dword v31, v[134:135], off nt
	s_waitcnt vmcnt(0)
